# P0: bf16 XB/MEMB stores of the conversion pass issued with sc1 (write-through), on top of the nt streaming loads
# speedup vs baseline: 1.0420x; 1.0041x over previous
.LBB0_70:
	s_and_b64 s[16:17], s[16:17], exec
	s_cselect_b32 s16, s68, s70
	s_cselect_b32 s17, s3, s69
	s_lshl_b64 s[14:15], s[14:15], 11
	s_add_u32 s14, s17, s14
	s_addc_u32 s15, s16, s15
	v_lshlrev_b32_e32 v82, 3, v198
	s_waitcnt vmcnt(3)
	v_cvt_pk_bf16_f32 v78, v78, v79
	v_cvt_pk_bf16_f32 v79, v80, v81
	s_waitcnt vmcnt(2)
	v_cvt_pk_bf16_f32 v74, v74, v75
	v_cvt_pk_bf16_f32 v75, v76, v77
	s_waitcnt vmcnt(1)
	v_cvt_pk_bf16_f32 v70, v70, v71
	v_cvt_pk_bf16_f32 v71, v72, v73
	s_waitcnt vmcnt(0)
	v_cvt_pk_bf16_f32 v66, v66, v67
	v_cvt_pk_bf16_f32 v67, v68, v69
	s_andn2_b64 vcc, exec, s[12:13]
	global_store_dwordx2 v82, v[78:79], s[14:15] sc1
	global_store_dwordx2 v82, v[74:75], s[14:15] offset:512 sc1
	global_store_dwordx2 v82, v[70:71], s[14:15] offset:1024 sc1
	global_store_dwordx2 v82, v[66:67], s[14:15] offset:1536 sc1
	s_cbranch_vccnz .LBB0_74
	s_ashr_i32 s12, s30, 31
	s_cmpk_lt_i32 s30, 0x4000
	s_cselect_b32 s13, s12, 0
	s_cselect_b32 s12, s30, s29
	s_cselect_b32 s14, s68, s70
	s_cselect_b32 s15, s3, s69
	s_lshl_b64 s[12:13], s[12:13], 11
	s_add_u32 s12, s15, s12
	s_addc_u32 s13, s14, s13
	v_cvt_pk_bf16_f32 v66, v62, v63
	v_cvt_pk_bf16_f32 v67, v64, v65
	global_store_dwordx2 v82, v[66:67], s[12:13] sc1
	v_cvt_pk_bf16_f32 v66, v58, v59
	v_cvt_pk_bf16_f32 v67, v60, v61
	global_store_dwordx2 v82, v[66:67], s[12:13] offset:512 sc1
	v_cvt_pk_bf16_f32 v66, v54, v55
	v_cvt_pk_bf16_f32 v67, v56, v57
	global_store_dwordx2 v82, v[66:67], s[12:13] offset:1024 sc1
	v_cvt_pk_bf16_f32 v66, v50, v51
	v_cvt_pk_bf16_f32 v67, v52, v53
	global_store_dwordx2 v82, v[66:67], s[12:13] offset:1536 sc1
	s_andn2_b64 vcc, exec, s[10:11]
	s_cbranch_vccz .LBB0_75

.LBB0_73:
	s_ashr_i32 s4, s26, 31
	s_cmpk_lt_i32 s26, 0x4000
	s_cselect_b32 s5, s4, 0
	s_cselect_b32 s4, s26, s25
	s_cselect_b32 s10, s68, s70
	s_cselect_b32 s11, s3, s69
	s_lshl_b64 s[4:5], s[4:5], 11
	s_add_u32 s4, s11, s4
	s_addc_u32 s5, s10, s5
	v_cvt_pk_bf16_f32 v66, v30, v31
	v_cvt_pk_bf16_f32 v67, v32, v33
	global_store_dwordx2 v82, v[66:67], s[4:5] sc1
	v_cvt_pk_bf16_f32 v66, v26, v27
	v_cvt_pk_bf16_f32 v67, v28, v29
	global_store_dwordx2 v82, v[66:67], s[4:5] offset:512 sc1
	v_cvt_pk_bf16_f32 v66, v22, v23
	v_cvt_pk_bf16_f32 v67, v24, v25
	global_store_dwordx2 v82, v[66:67], s[4:5] offset:1024 sc1
	v_cvt_pk_bf16_f32 v66, v18, v19
	v_cvt_pk_bf16_f32 v67, v20, v21
	global_store_dwordx2 v82, v[66:67], s[4:5] offset:1536 sc1
	s_andn2_b64 vcc, exec, s[0:1]
	s_cbranch_vccnz .LBB0_61
	s_branch .LBB0_77

.LBB0_75:
	s_ashr_i32 s10, s28, 31
	s_cmpk_lt_i32 s28, 0x4000
	s_cselect_b32 s11, s10, 0
	s_cselect_b32 s10, s28, s27
	s_cselect_b32 s12, s68, s70
	s_cselect_b32 s13, s3, s69
	s_lshl_b64 s[10:11], s[10:11], 11
	s_add_u32 s10, s13, s10
	s_addc_u32 s11, s12, s11
	v_cvt_pk_bf16_f32 v66, v46, v47
	v_cvt_pk_bf16_f32 v67, v48, v49
	global_store_dwordx2 v82, v[66:67], s[10:11] sc1
	v_cvt_pk_bf16_f32 v66, v42, v43
	v_cvt_pk_bf16_f32 v67, v44, v45
	global_store_dwordx2 v82, v[66:67], s[10:11] offset:512 sc1
	v_cvt_pk_bf16_f32 v66, v38, v39
	v_cvt_pk_bf16_f32 v67, v40, v41
	global_store_dwordx2 v82, v[66:67], s[10:11] offset:1024 sc1
	v_cvt_pk_bf16_f32 v66, v34, v35
	v_cvt_pk_bf16_f32 v67, v36, v37
	global_store_dwordx2 v82, v[66:67], s[10:11] offset:1536 sc1
	s_andn2_b64 vcc, exec, s[4:5]
	s_cbranch_vccz .LBB0_73

.LBB0_77:
	s_ashr_i32 s0, s24, 31
	s_cmpk_lt_i32 s24, 0x4000
	s_cselect_b32 s1, s0, 0
	s_cselect_b32 s0, s24, s23
	s_cselect_b32 s4, s68, s70
	s_cselect_b32 s5, s3, s69
	s_lshl_b64 s[0:1], s[0:1], 11
	s_add_u32 s0, s5, s0
	s_addc_u32 s1, s4, s1
	v_cvt_pk_bf16_f32 v66, v14, v15
	v_cvt_pk_bf16_f32 v67, v16, v17
	global_store_dwordx2 v82, v[66:67], s[0:1] sc1
	v_cvt_pk_bf16_f32 v66, v10, v11
	v_cvt_pk_bf16_f32 v67, v12, v13
	global_store_dwordx2 v82, v[66:67], s[0:1] offset:512 sc1
	v_cvt_pk_bf16_f32 v66, v6, v7
	v_cvt_pk_bf16_f32 v67, v8, v9
	global_store_dwordx2 v82, v[66:67], s[0:1] offset:1024 sc1
	v_cvt_pk_bf16_f32 v66, v2, v3
	v_cvt_pk_bf16_f32 v67, v4, v5
	global_store_dwordx2 v82, v[66:67], s[0:1] offset:1536 sc1
	s_branch .LBB0_61
